# E26: E21 + forget-gate cumsum moved from prep (blockIdx<32 critical path) to idle tail WGs of the in-proj GEMM phase
# baseline (speedup 1.0000x reference)
.LBB0_187:
	s_cmpk_lt_i32 s80, 0x2c0
	s_cselect_b64 s[0:1], -1, 0
	v_writelane_b32 v251, s0, 2
	s_add_i32 s2, s78, 0x2bf
	s_sub_i32 s3, s2, s80
	v_writelane_b32 v251, s1, 3
	s_mul_hi_i32 s0, s80, 0x2e8ba2e9
	s_lshr_b32 s1, s0, 31
	s_ashr_i32 s0, s0, 1
	s_add_i32 s12, s0, s1
	s_mul_i32 s0, s12, 11
	s_sub_i32 s18, s80, s0
	s_add_u32 s88, s4, 0x4200
	s_addc_u32 s89, s5, 0
	s_add_u32 s90, s4, 0x4400
	s_addc_u32 s91, s5, 0
	s_add_u32 s92, s4, 0x4500
	s_addc_u32 s93, s5, 0
	s_add_u32 s94, s4, 0x4600
	s_addc_u32 s95, s5, 0
	s_add_u32 s96, s4, 0x4700
	s_addc_u32 s97, s5, 0
	s_add_u32 s72, s4, 0x4800
	s_addc_u32 s73, s5, 0
	s_add_u32 s74, s4, 0x4900
	s_addc_u32 s75, s5, 0
	s_add_u32 s0, s4, 0x4a00
	s_addc_u32 s1, s5, 0
	v_writelane_b32 v251, s0, 4
	s_mov_b32 s17, 0
	s_mov_b32 s10, s50
	v_writelane_b32 v251, s1, 5
	s_add_u32 s0, s4, 0x4b00
	s_addc_u32 s1, s5, 0
	v_writelane_b32 v251, s0, 6
	s_mov_b32 s11, s17
	v_mov_b32_e32 v101, 0
	v_writelane_b32 v251, s1, 7
	s_add_u32 s0, s4, 0x4c00
	s_addc_u32 s1, s5, 0
	v_writelane_b32 v251, s0, 8
	v_mov_b32_e32 v210, 1
	v_mov_b32_e32 v212, 0x260
	v_writelane_b32 v251, s1, 9
	s_add_u32 s0, s4, 0x4d00
	s_addc_u32 s1, s5, 0
	v_writelane_b32 v251, s0, 10
	v_mov_b32_e32 v214, 0x3a27c5ac
	v_mov_b32_e32 v215, 0x358637bd
	v_writelane_b32 v251, s1, 11
	s_add_u32 s0, s4, 0x4e00
	s_addc_u32 s1, s5, 0
	v_writelane_b32 v251, s0, 12
	v_mov_b32_e32 v213, 0x200000
	v_mov_b32_e32 v218, 0x3e38aa3b
	v_writelane_b32 v251, s1, 13
	s_add_u32 s0, s4, 0x4f00
	s_addc_u32 s1, s5, 0
	v_writelane_b32 v251, s0, 14
	v_mov_b32_e32 v219, 0x7f800000
	v_mov_b32_e32 v220, 0x7fc00000
	v_writelane_b32 v251, s1, 15
	s_add_u32 s0, s4, 0x5000
	s_addc_u32 s1, s5, 0
	v_writelane_b32 v251, s0, 16
	v_mov_b32_e32 v221, 0xff800000
	v_mov_b32_e32 v223, 0xfcf
	v_writelane_b32 v251, s1, 17
	s_add_u32 s0, s4, 0x5100
	s_addc_u32 s1, s5, 0
	v_writelane_b32 v251, s0, 18
	v_mov_b32_e32 v224, 0x380
	v_mov_b32_e32 v225, 0x41b17218
	v_writelane_b32 v251, s1, 19
	s_add_u32 s0, s4, 0x5200
	s_addc_u32 s1, s5, 0
	v_writelane_b32 v251, s0, 20
	v_mov_b32_e32 v226, 0x3fb8aa3b
	v_mov_b32_e32 v227, 1.0
	v_writelane_b32 v251, s1, 21
	s_add_u32 s0, s4, 0x5300
	s_addc_u32 s1, s5, 0
	v_writelane_b32 v251, s0, 22
	s_cmp_eq_u32 s33, 15
	v_mov_b32_e32 v250, 0x3f803f80
	v_writelane_b32 v251, s1, 23
	s_cselect_b64 s[0:1], -1, 0
	v_writelane_b32 v251, s0, 24
	s_cmp_eq_u32 s33, 14
	v_mov_b32_e32 v211, 0x200
	v_writelane_b32 v251, s1, 25
	s_cselect_b64 s[0:1], -1, 0
	v_writelane_b32 v251, s0, 26
	s_cmp_eq_u32 s33, 13
	v_mov_b32_e32 v230, 0x40e00000
	v_writelane_b32 v251, s1, 27
	s_cselect_b64 s[0:1], -1, 0
	v_writelane_b32 v251, s0, 28
	s_cmp_eq_u32 s33, 12
	s_movk_i32 s76, 0x6000
	v_writelane_b32 v251, s1, 29
	s_cselect_b64 s[0:1], -1, 0
	v_writelane_b32 v251, s0, 30
	s_cmp_eq_u32 s33, 11
	s_movk_i32 s58, 0x380
	v_writelane_b32 v251, s1, 31
	s_cselect_b64 s[0:1], -1, 0
	v_writelane_b32 v251, s0, 32
	s_cmp_eq_u32 s33, 10
	s_mov_b32 s59, 0xf800000
	v_writelane_b32 v251, s1, 33
	s_cselect_b64 s[0:1], -1, 0
	v_writelane_b32 v251, s0, 34
	s_cmp_eq_u32 s33, 9
	s_mov_b32 s60, 0x800000
	v_writelane_b32 v251, s1, 35
	s_cselect_b64 s[0:1], -1, 0
	v_writelane_b32 v251, s0, 36
	s_cmp_eq_u32 s33, 8
	s_mov_b32 s61, 0x3f317217
	v_writelane_b32 v251, s1, 37
	s_cselect_b64 s[0:1], -1, 0
	v_writelane_b32 v251, s0, 38
	s_cmp_eq_u32 s33, 7
	s_movk_i32 s34, 0x7000
	v_writelane_b32 v251, s1, 39
	s_cselect_b64 s[0:1], -1, 0
	v_writelane_b32 v251, s0, 40
	s_cmp_eq_u32 s33, 6
	s_movk_i32 s35, 0x3000
	v_writelane_b32 v251, s1, 41
	s_cselect_b64 s[0:1], -1, 0
	v_writelane_b32 v251, s0, 42
	s_cmp_eq_u32 s33, 5
	s_movk_i32 s69, 0x5000
	v_writelane_b32 v251, s1, 43
	s_cselect_b64 s[0:1], -1, 0
	v_writelane_b32 v251, s0, 44
	s_cmp_eq_u32 s33, 4
	s_mov_b32 s62, 0x41800000
	v_writelane_b32 v251, s1, 45
	s_cselect_b64 s[0:1], -1, 0
	v_writelane_b32 v251, s0, 46
	s_cmp_eq_u32 s33, 3
	s_mov_b32 s63, 0xc0e00000
	v_writelane_b32 v251, s1, 47
	s_cselect_b64 s[0:1], -1, 0
	v_writelane_b32 v251, s0, 48
	s_cmp_eq_u32 s33, 2
	s_mov_b32 s54, s17
	v_writelane_b32 v251, s1, 49
	s_cselect_b64 s[0:1], -1, 0
	v_writelane_b32 v251, s0, 50
	s_cmp_eq_u32 s33, 1
	s_nop 0
	v_writelane_b32 v251, s1, 51
	s_cselect_b64 s[0:1], -1, 0
	v_writelane_b32 v251, s0, 52
	s_cmp_eq_u32 s33, 0
	s_nop 0
	v_writelane_b32 v251, s1, 53
	s_cselect_b64 s[0:1], -1, 0
	v_writelane_b32 v251, s0, 54
	s_nop 1
	v_writelane_b32 v251, s1, 55
	s_lshl_b32 s0, s33, 8
	s_add_u32 s0, s6, s0
	s_addc_u32 s1, s7, 0
	s_add_u32 s6, s0, 0x1400
	s_addc_u32 s7, s1, 0
	v_writelane_b32 v251, s6, 56
	s_add_u32 s0, s0, 0x2400
	s_addc_u32 s1, s1, 0
	v_writelane_b32 v251, s7, 57
	v_writelane_b32 v251, s0, 58
	s_movk_i32 s33, 0x7fff
	s_nop 0
	v_writelane_b32 v251, s1, 59
	s_add_u32 s0, s4, 0x7400
	s_addc_u32 s1, s5, 0
	v_writelane_b32 v251, s0, 60
	s_nop 1
	v_writelane_b32 v251, s1, 61
	s_add_u32 s0, s4, 0x7500
	s_addc_u32 s1, s5, 0
	v_writelane_b32 v251, s0, 62
	s_cmp_lt_u32 s50, 32
	s_nop 0
	v_writelane_b32 v251, s1, 63
	s_cselect_b64 s[0:1], -1, 0
	v_writelane_b32 v252, s0, 0
	s_nop 1
	v_writelane_b32 v252, s1, 1
	s_lshl_b32 s0, s50, 11
	s_and_b32 s0, s0, 0x60000
	s_bfe_u32 s1, s50, 0x30003
	v_writelane_b32 v252, s0, 2
	v_writelane_b32 v252, s1, 3
	s_lshl_b32 s0, s1, 14
	v_writelane_b32 v252, s0, 4
	s_and_b32 s0, s50, 7
	s_cmp_eq_u32 s0, 6
	s_cselect_b32 s0, 1, 0
	s_nop 0
	v_writelane_b32 v255, s0, 63
	s_cmpk_lt_i32 s80, 0xc0
	s_mul_hi_i32 s0, s80, 0x55555556
	s_cselect_b64 s[4:5], -1, 0
	s_lshr_b32 s1, s0, 31
	s_add_i32 s20, s0, s1
	s_mul_i32 s0, s20, 3
	s_sub_i32 s22, s80, s0
	v_writelane_b32 v252, s4, 5
	s_cmpk_gt_i32 s80, 0xbf
	s_cselect_b64 s[0:1], -1, 0
	v_writelane_b32 v252, s5, 6
	v_writelane_b32 v252, s0, 7
	s_nop 1
	v_writelane_b32 v252, s1, 8
	s_ashr_i32 s0, s80, 6
	s_ashr_i32 s1, s0, 31
	s_lshl_b64 s[4:5], s[0:1], 12
	s_lshl_b32 s0, s80, 6
	v_writelane_b32 v252, s0, 9
	s_and_b32 s0, s0, 0xfc0
	s_or_b32 s4, s4, s0
	v_writelane_b32 v252, s4, 10
	s_cmpk_lt_i32 s80, 0x400
	s_cselect_b64 s[0:1], -1, 0
	v_writelane_b32 v252, s5, 11
	v_writelane_b32 v252, s0, 12
	s_cmp_lt_u32 s50, 16
	s_nop 0
	v_writelane_b32 v252, s1, 13
	s_cselect_b64 s[0:1], -1, 0
	v_writelane_b32 v252, s0, 14
	s_nop 1
	v_writelane_b32 v252, s1, 15
	s_lshl_b64 s[0:1], s[10:11], 19
	s_cmpk_lg_i32 s78, 0x100
	s_cselect_b64 s[4:5], -1, 0
	v_writelane_b32 v252, s4, 16
	s_cmpk_lt_i32 s80, 0x200
	s_nop 0
	v_writelane_b32 v252, s5, 17
	s_cselect_b64 s[4:5], -1, 0
	v_writelane_b32 v252, s4, 18
	s_nop 1
	v_writelane_b32 v252, s5, 19
	s_add_i32 s4, s80, s78
	s_lshl_b32 s5, s4, 1
	v_writelane_b32 v252, s5, 20
	s_lshl_b32 s5, s80, 1
	s_cmpk_lt_i32 s80, 0x100
	s_cselect_b64 s[6:7], -1, 0
	s_ashr_i32 s81, s80, 31
	v_writelane_b32 v252, s5, 21
	s_lshr_b32 s5, s81, 30
	v_writelane_b32 v252, s6, 22
	s_add_i32 s5, s80, s5
	s_ashr_i32 s8, s5, 2
	v_writelane_b32 v252, s7, 23
	s_and_b32 s6, s5, -4
	s_sub_i32 s14, s80, s6
	s_mov_b32 s6, s8
	s_ashr_i32 s9, s8, 31
	v_writelane_b32 v252, s6, 24
	s_ashr_i32 s15, s14, 31
	s_nop 0
	v_writelane_b32 v252, s7, 25
	s_lshl_b64 s[6:7], s[8:9], 19
	v_writelane_b32 v252, s6, 26
	s_nop 1
	v_writelane_b32 v252, s7, 27
	s_mov_b32 s6, s14
	v_writelane_b32 v252, s6, 28
	s_nop 1
	v_writelane_b32 v252, s7, 29
	s_lshl_b64 s[6:7], s[14:15], 19
	v_writelane_b32 v252, s6, 30
	s_cmpk_lt_i32 s50, 0x100
	s_mov_b32 s14, s12
	v_writelane_b32 v252, s7, 31
	s_cselect_b64 s[6:7], -1, 0
	s_and_b32 s5, s78, 63
	v_writelane_b32 v252, s6, 32
	s_cmp_eq_u32 s5, 0
	s_nop 0
	v_writelane_b32 v252, s7, 33
	s_cselect_b64 s[6:7], -1, 0
	s_abs_i32 s9, s78
	v_cvt_f32_u32_e32 v1, s9
	v_writelane_b32 v252, s6, 34
	s_sub_i32 s5, 0, s9
	s_ashr_i32 s15, s78, 3
	v_rcp_iflag_f32_e32 v1, v1
	v_writelane_b32 v252, s7, 35
	s_ashr_i32 s13, s12, 31
	s_lshl_b64 s[12:13], s[12:13], 19
	v_mul_f32_e32 v1, 0x4f7ffffe, v1
	v_cvt_u32_f32_e32 v1, v1
	s_ashr_i32 s19, s18, 31
	s_ashr_i32 s21, s20, 31
	s_ashr_i32 s23, s22, 31
	v_readfirstlane_b32 s6, v1
	s_mul_i32 s5, s5, s6
	s_mul_hi_u32 s5, s6, s5
	s_add_i32 s11, s6, s5
	s_abs_i32 s5, s3
	s_mul_hi_u32 s6, s5, s11
	s_mul_i32 s7, s6, s9
	s_sub_i32 s5, s5, s7
	s_add_i32 s7, s78, -1
	v_writelane_b32 v252, s7, 36
	v_writelane_b32 v252, s14, 37
	s_ashr_i32 s3, s3, 31
	s_ashr_i32 s79, s78, 31
	v_writelane_b32 v252, s15, 38
	v_writelane_b32 v252, s12, 39
	s_xor_b32 s3, s3, s79
	s_add_i32 s7, s6, 1
	v_writelane_b32 v252, s13, 40
	s_mov_b32 s12, s18
	v_writelane_b32 v252, s12, 41
	s_sub_i32 s8, s5, s9
	s_nop 0
	v_writelane_b32 v252, s13, 42
	s_lshl_b64 s[12:13], s[18:19], 19
	v_writelane_b32 v252, s12, 43
	s_nop 1
	v_writelane_b32 v252, s13, 44
	s_mov_b32 s12, s20
	v_writelane_b32 v252, s12, 45
	s_nop 1
	v_writelane_b32 v252, s13, 46
	s_lshl_b64 s[12:13], s[20:21], 17
	v_writelane_b32 v252, s12, 47
	s_mov_b64 s[20:21], 0x80
	s_nop 0
	v_writelane_b32 v252, s13, 48
	s_mov_b32 s12, s22
	v_writelane_b32 v252, s12, 49
	s_nop 1
	v_writelane_b32 v252, s13, 50
	s_lshl_b64 s[12:13], s[22:23], 17
	s_cmp_ge_u32 s5, s9
	s_cselect_b32 s6, s7, s6
	s_cselect_b32 s5, s8, s5
	s_add_i32 s7, s6, 1
	s_cmp_ge_u32 s5, s9
	s_cselect_b32 s5, s7, s6
	s_xor_b32 s5, s5, s3
	s_sub_i32 s3, s5, s3
	s_sub_i32 s5, 0xfffffd41, s78
	s_max_i32 s5, s2, s5
	s_mul_hi_u32 s6, s5, s11
	s_mul_i32 s7, s6, s9
	s_sub_i32 s5, s5, s7
	s_ashr_i32 s2, s2, 31
	s_xor_b32 s2, s2, s79
	s_add_i32 s7, s6, 1
	s_sub_i32 s8, s5, s9
	s_cmp_ge_u32 s5, s9
	s_cselect_b32 s6, s7, s6
	s_cselect_b32 s5, s8, s5
	s_add_i32 s7, s6, 1
	s_cmp_ge_u32 s5, s9
	s_cselect_b32 s5, s7, s6
	s_xor_b32 s5, s5, s2
	s_sub_i32 s2, s5, s2
	s_cmp_gt_i32 s2, s3
	s_cselect_b64 s[6:7], -1, 0
	s_sub_i32 s8, s2, s3
	s_abs_i32 s2, s15
	v_cvt_f32_u32_e32 v1, s2
	v_writelane_b32 v252, s12, 51
	s_sub_i32 s3, 0, s2
	s_mov_b32 s23, 0x7f800000
	v_rcp_iflag_f32_e32 v1, v1
	v_writelane_b32 v252, s13, 52
	v_writelane_b32 v252, s11, 53
	v_writelane_b32 v252, s9, 54
	v_mul_f32_e32 v1, 0x4f7ffffe, v1
	v_cvt_u32_f32_e32 v1, v1
	v_writelane_b32 v252, s6, 55
	s_mov_b32 s22, 0xbfb8aa3b
	v_readfirstlane_b32 s5, v1
	s_mul_i32 s3, s3, s5
	s_mul_hi_u32 s3, s5, s3
	s_add_i32 s5, s5, s3
	s_abs_i32 s3, s80
	s_mul_hi_u32 s5, s3, s5
	v_writelane_b32 v252, s7, 56
	s_mul_i32 s6, s5, s2
	s_sub_i32 s3, s3, s6
	s_sub_i32 s6, s3, s2
	s_add_i32 s7, s5, 1
	s_cmp_ge_u32 s3, s2
	s_cselect_b32 s3, s6, s3
	s_cselect_b32 s5, s7, s5
	s_sub_i32 s6, s3, s2
	s_add_i32 s7, s5, 1
	s_cmp_ge_u32 s3, s2
	s_cselect_b32 s2, s6, s3
	s_cselect_b32 s3, s7, s5
	s_xor_b32 s5, s81, s79
	s_xor_b32 s2, s2, s81
	s_xor_b32 s3, s3, s5
	s_sub_i32 s2, s2, s81
	s_sub_i32 s3, s3, s5
	v_writelane_b32 v252, s2, 57
	v_writelane_b32 v252, s15, 58
	s_mul_i32 s2, s3, s15
	v_writelane_b32 v252, s3, 59
	s_sub_i32 s2, s80, s2
	v_writelane_b32 v252, s2, 60
	s_lshl_b32 s2, s4, 6
	v_writelane_b32 v252, s2, 61
	s_lshl_b64 s[4:5], s[80:81], 13
	v_writelane_b32 v252, s4, 62
	s_lshl_b32 s2, s78, 6
	v_mbcnt_lo_u32_b32 v1, -1, 0
	v_writelane_b32 v252, s5, 63
	s_lshl_b64 s[4:5], s[78:79], 13
	v_writelane_b32 v253, s4, 0
	v_mbcnt_hi_u32_b32 v222, -1, v1
	s_nop 0
	v_writelane_b32 v253, s5, 1
	s_lshl_b64 s[4:5], s[80:81], 14
	v_writelane_b32 v253, s4, 2
	s_mov_b32 s81, s8
	s_nop 0
	v_writelane_b32 v253, s5, 3
	s_lshl_b64 s[4:5], s[78:79], 14
	v_writelane_b32 v253, s4, 4
	s_add_u32 s0, s0, 0x5f000000
	s_addc_u32 s1, s1, 0
	v_writelane_b32 v253, s5, 5
	v_writelane_b32 v253, s0, 6
	s_nop 1
	v_writelane_b32 v253, s1, 7
	s_mul_hi_i32 s1, s80, 0x6000
	s_mul_i32 s0, s80, 0x6000
	v_writelane_b32 v253, s0, 8
	s_nop 1
	v_writelane_b32 v253, s1, 9
	s_mul_hi_i32 s1, s78, 0x6000
	s_mul_i32 s0, s78, 0x6000
	v_writelane_b32 v253, s0, 10
	s_nop 1
	v_writelane_b32 v253, s1, 11
	s_mul_i32 s1, s50, 0x180000
	v_writelane_b32 v253, s1, 12
	s_add_u32 s1, s1, 0x5c012000
	s_mul_hi_u32 s0, s50, 0x180000
	v_writelane_b32 v253, s1, 13
	v_writelane_b32 v253, s0, 14
	s_addc_u32 s0, s0, 0
	v_writelane_b32 v253, s0, 15
	s_mov_b32 s0, s50
	v_writelane_b32 v253, s0, 16
	s_ashr_i32 s87, s86, 31
	s_lshl_b32 s36, s78, 1
	v_writelane_b32 v253, s1, 17
	s_lshl_b32 s0, s50, 6
	s_or_b32 s0, s0, 3
	v_writelane_b32 v253, s0, 18
	s_lshl_b32 s0, s80, 7
	v_writelane_b32 v253, s0, 19
	s_add_i32 s0, s77, s86
	v_writelane_b32 v253, s0, 20
	s_add_i32 s0, 0, 0x221f0
	v_writelane_b32 v253, s0, 21
	s_add_i32 s0, 0, 0x22040
	v_writelane_b32 v253, s0, 22
	s_add_i32 s0, 0, 0x221d0
	v_writelane_b32 v253, s0, 23
	s_add_i32 s0, 0, 0x221c0
	v_writelane_b32 v253, s0, 24
	s_add_i32 s0, 0, 0x22020
	v_writelane_b32 v253, s0, 25
	s_add_i32 s0, 0, 0x22024
	v_writelane_b32 v253, s0, 26
	s_add_i32 s0, 0, 0x221a0
	v_writelane_b32 v253, s0, 27
	s_add_i32 s0, 0, 0x22138
	v_writelane_b32 v253, s0, 28
	s_add_i32 s0, 0, 0x22168
	v_writelane_b32 v253, s0, 29
	s_add_i32 s0, 0, 0x22140
	v_writelane_b32 v253, s0, 30
	s_add_i32 s0, 0, 0x22150
	v_writelane_b32 v253, s0, 31
	s_add_i32 s0, 0, 0x22170
	v_writelane_b32 v253, s0, 32
	s_add_i32 s0, 0, 0x23800
	v_writelane_b32 v253, s0, 33
	s_add_i32 s0, 0, 0x1b000
	v_writelane_b32 v253, s0, 34
	s_add_i32 s0, 0, 0x13240
	v_writelane_b32 v253, s0, 35
	s_add_i32 s0, 0, 0x13200
	v_writelane_b32 v253, s0, 36
	s_add_i32 s0, 0, 0x22190
	v_writelane_b32 v253, s0, 37
	s_add_i32 s0, 0, 0x22198
	v_writelane_b32 v253, s0, 38
	s_add_i32 s0, 0, 0x22100
	v_writelane_b32 v253, s0, 39
	s_add_i32 s0, 0, 0x221a8
	v_writelane_b32 v253, s0, 40
	s_add_i32 s0, 0, 0x221b8
	v_writelane_b32 v253, s0, 41
	s_add_i32 s0, 0, 0x22200
	v_writelane_b32 v253, s0, 42
	s_add_i32 s0, 0, 0x22280
	v_writelane_b32 v253, s0, 43
	s_add_i32 s0, 0, 0x22300
	v_writelane_b32 v253, s0, 44
	s_add_i32 s0, 0, 0x22700
	v_writelane_b32 v253, s0, 45
	s_add_i32 s0, 0, 0x22c80
	v_writelane_b32 v253, s0, 46
	s_add_i32 s0, 0, 0x22044
	v_writelane_b32 v253, s0, 47
	s_add_i32 s0, 0, 0x221c8
	v_writelane_b32 v253, s0, 48
	s_add_i32 s0, 0, 0x23000
	v_writelane_b32 v253, s0, 49
	s_add_i32 s0, 0, 0x221d8
	v_writelane_b32 v253, s0, 50
	s_add_i32 s0, 0, 0x22128
	v_writelane_b32 v253, s0, 51
	s_add_i32 s0, 0, 0x22120
	v_writelane_b32 v253, s0, 52
	s_add_i32 s0, 0, 0x221e0
	v_writelane_b32 v253, s0, 53
	s_add_i32 s0, 0, 0x221e8
	v_writelane_b32 v253, s0, 54
	s_lshl_b64 s[0:1], s[86:87], 11
	v_writelane_b32 v253, s0, 55
	s_lshl_b32 s37, s78, 7
	s_add_i32 s70, 0, 0x22178
	v_writelane_b32 v253, s1, 56
	s_lshl_b64 s[0:1], s[86:87], 5
	v_writelane_b32 v253, s0, 57
	s_add_i32 s71, 0, 0x22188
	s_nop 0
	v_writelane_b32 v253, s1, 58
	s_lshl_b64 s[0:1], s[86:87], 12
	v_writelane_b32 v253, s0, 59
	s_nop 1
	v_writelane_b32 v253, s1, 60
	s_lshl_b64 s[0:1], s[86:87], 13
	v_writelane_b32 v253, s0, 61
	s_mov_b32 s87, s2
	s_nop 0
	v_writelane_b32 v253, s1, 62
	v_writelane_b32 v253, s72, 63
	s_nop 1
	v_writelane_b32 v254, s73, 0
	v_writelane_b32 v254, s74, 1
	s_nop 1
	v_writelane_b32 v254, s75, 2
	v_writelane_b32 v254, s36, 3
	v_writelane_b32 v254, s37, 4
	v_writelane_b32 v254, s70, 5
	v_writelane_b32 v254, s71, 6
	v_writelane_b32 v254, s80, 7
	s_nop 1
	v_writelane_b32 v254, s81, 8
	v_writelane_b32 v254, s82, 9
	s_nop 1
	v_writelane_b32 v254, s83, 10
	v_writelane_b32 v254, s84, 11
	s_nop 1
	v_writelane_b32 v254, s85, 12
	v_writelane_b32 v254, s77, 13
	v_writelane_b32 v254, s86, 14
	s_nop 1
	v_writelane_b32 v254, s87, 15
	v_writelane_b32 v254, s88, 16
	s_nop 1
	v_writelane_b32 v254, s89, 17
	v_writelane_b32 v254, s90, 18
	s_nop 1
	v_writelane_b32 v254, s91, 19
	v_writelane_b32 v254, s92, 20
	s_nop 1
	v_writelane_b32 v254, s93, 21
	v_writelane_b32 v254, s94, 22
	s_nop 1
	v_writelane_b32 v254, s95, 23
	v_writelane_b32 v254, s96, 24
	s_nop 1
	v_writelane_b32 v254, s97, 25
	v_writelane_b32 v254, s81, 26
	v_writelane_b32 v254, s87, 27

.LBB0_377:
	s_barrier
	v_readlane_b32 s0, v255, 63
	s_nop 3
	s_cmp_lg_u32 s0, 1
	s_cbranch_scc1 .Lcs_return
	v_readlane_b32 s0, v253, 21
	s_nop 0
	v_readfirstlane_b32 s5, v0
	v_mov_b32_e32 v1, s0
	s_waitcnt vmcnt(0)
	ds_read_b64 v[2:3], v1
	v_and_b32_e32 v22, 63, v0
	s_nop 3
	s_ashr_i32 s4, s5, 6
	s_waitcnt lgkmcnt(0)
	v_readfirstlane_b32 s3, v3
	v_readfirstlane_b32 s2, v2
	s_nop 3
	s_branch .Lcs_entry
.Lcs_return:
.LBB0_378:
	s_mul_i32 s0, s54, 9
	s_add_i32 s16, s0, 3
	s_cmp_ge_i32 s16, s85
	s_movk_i32 s34, 0x7000
	s_cbranch_scc1 .LBB0_432
	s_waitcnt vmcnt(0)
	s_waitcnt vmcnt(0)
	s_barrier
	s_and_saveexec_b64 s[0:1], s[82:83]
	s_cbranch_execz .LBB0_431
	v_readlane_b32 s2, v253, 25
	s_waitcnt vmcnt(0) expcnt(0) lgkmcnt(0)
	s_nop 0
	v_mov_b32_e32 v1, s2
	ds_read_b32 v3, v1
	v_readlane_b32 s2, v253, 26
	s_waitcnt lgkmcnt(0)
	v_cmp_ne_u32_e32 vcc, 0, v3
	v_mov_b32_e32 v1, s2
	ds_read_b32 v2, v1
	s_cbranch_vccnz .LBB0_395
	v_readlane_b32 s4, v251, 0
	v_readlane_b32 s5, v251, 1
	s_load_dwordx2 s[2:3], s[4:5], 0x4
	s_mov_b32 s9, 1
	s_waitcnt lgkmcnt(0)
	s_mul_i32 s8, s2, s78
	s_mul_i32 s8, s8, s3
	s_branch .LBB0_383

.LBB0_434:
	s_andn2_b64 vcc, exec, s[0:1]
	s_mov_b32 s0, s54
	v_writelane_b32 v254, s0, 29
	s_nop 1
	v_writelane_b32 v254, s1, 30
	s_cbranch_vccnz .LBB0_762
	v_readlane_b32 s0, v253, 21
	s_nop 0
	v_readfirstlane_b32 s5, v0
	v_mov_b32_e32 v1, s0
	s_waitcnt vmcnt(0)
	ds_read_b64 v[2:3], v1
	v_readlane_b32 s0, v252, 0
	v_readlane_b32 s1, v252, 1
	v_and_b32_e32 v22, 63, v0
	s_ashr_i32 s4, s5, 6
	s_waitcnt lgkmcnt(0)
	v_readfirstlane_b32 s3, v3
	s_andn2_b64 vcc, exec, s[0:1]
	v_readfirstlane_b32 s2, v2
	s_branch .LBB0_446
.Lcs_entry:
	v_readlane_b32 s0, v253, 27
	v_readlane_b32 s8, v252, 3
	s_nop 0
	v_mov_b32_e32 v1, s0
	ds_read_b64 v[2:3], v1
	s_lshl_b32 s0, s54, 3
	s_or_b32 s16, s0, s8
	s_lshl_b64 s[0:1], s[16:17], 2
	s_waitcnt lgkmcnt(0)
	v_readfirstlane_b32 s7, v2
	v_readfirstlane_b32 s6, v3
	s_add_u32 s0, s7, s0
	s_addc_u32 s1, s6, s1
	global_load_dword v8, v101, s[0:1]
	v_lshlrev_b32_e32 v2, 3, v0
	v_readlane_b32 s0, v252, 2
	v_ashrrev_i32_e32 v3, 31, v2
	s_add_u32 s0, s2, s0
	s_addc_u32 s1, s3, 0
	v_lshlrev_b64 v[4:5], 5, v[2:3]
	v_lshl_add_u64 v[4:5], s[0:1], 0, v[4:5]
	s_lshl_b32 s16, s8, 2
	v_lshl_add_u64 v[4:5], v[4:5], 0, s[16:17]
	s_mov_b64 s[0:1], 0x200000
	v_lshl_add_u64 v[10:11], v[4:5], 0, s[0:1]
	s_mov_b32 s0, 0x200000
	v_add_co_u32_e32 v4, vcc, s0, v4
	s_mov_b32 s0, 0x3f2aaaab
	s_nop 0
	v_addc_co_u32_e32 v5, vcc, 0, v5, vcc
	global_load_dword v1, v[4:5], off
	global_load_dword v12, v[10:11], off offset:32
	s_nop 0
	global_load_dword v5, v[10:11], off offset:96
	global_load_dword v4, v[10:11], off offset:128
	global_load_dword v7, v[10:11], off offset:160
	global_load_dword v6, v[10:11], off offset:192
	global_load_dword v9, v[10:11], off offset:224
	global_load_dword v14, v[10:11], off offset:64
	s_mov_b32 s1, 0x3f317218
	s_mov_b32 s6, 0x33800000
	s_waitcnt vmcnt(7)
	v_add_f32_e32 v1, v8, v1
	v_mul_f32_e64 v11, |v1|, s22
	s_waitcnt vmcnt(6)
	v_add_f32_e32 v10, v8, v12
	v_exp_f32_e32 v15, v11
	v_mul_f32_e64 v12, |v10|, s22
	v_exp_f32_e32 v16, v12
	v_max_f32_e64 v17, -v10, 0
	v_add_f32_e32 v18, 1.0, v15
	v_frexp_mant_f32_e32 v21, v18
	v_cvt_f64_f32_e32 v[10:11], v18
	v_add_f32_e32 v19, 1.0, v16
	v_add_f32_e32 v20, -1.0, v18
	v_frexp_exp_i32_f64_e32 v10, v[10:11]
	v_cmp_gt_f32_e32 vcc, s0, v21
	v_cvt_f64_f32_e32 v[12:13], v19
	v_frexp_mant_f32_e32 v23, v19
	v_sub_f32_e32 v24, v20, v18
	v_subbrev_co_u32_e32 v10, vcc, 0, v10, vcc
	v_sub_f32_e32 v20, v15, v20
	v_frexp_exp_i32_f64_e32 v11, v[12:13]
	v_add_f32_e32 v12, 1.0, v24
	v_cmp_gt_f32_e32 vcc, s0, v23
	v_max_f32_e64 v1, -v1, 0
	s_waitcnt vmcnt(5)
	v_add_f32_e32 v5, v8, v5
	v_subbrev_co_u32_e32 v13, vcc, 0, v11, vcc
	v_add_f32_e32 v11, v20, v12
	v_sub_u32_e32 v12, 0, v10
	v_cvt_f32_i32_e32 v20, v13
	v_ldexp_f32 v18, v18, v12
	v_cvt_f32_i32_e32 v10, v10
	v_ldexp_f32 v11, v11, v12
	v_add_f32_e32 v12, -1.0, v18
	v_add_f32_e32 v21, 1.0, v18
	v_add_f32_e32 v23, 1.0, v12
	v_add_f32_e32 v24, -1.0, v21
	v_sub_f32_e32 v23, v18, v23
	v_sub_f32_e32 v18, v18, v24
	v_mul_f32_e32 v25, 0x3f317218, v20
	v_add_f32_e32 v23, v11, v23
	v_add_f32_e32 v11, v11, v18
	v_mul_f32_e32 v24, 0x3f317218, v10
	v_fma_f32 v26, v20, s1, -v25
	v_add_f32_e32 v28, v21, v11
	v_fma_f32 v18, v10, s1, -v24
	v_fmac_f32_e32 v26, 0xb102e308, v20
	v_rcp_f32_e32 v20, v28
	v_add_f32_e32 v27, v12, v23
	v_fmac_f32_e32 v18, 0xb102e308, v10
	v_sub_f32_e32 v10, v27, v12
	v_sub_f32_e32 v12, v28, v21
	v_add_f32_e32 v21, v24, v18
	v_sub_f32_e32 v11, v11, v12
	v_sub_f32_e32 v12, v21, v24
	v_sub_f32_e32 v12, v18, v12
	v_mul_f32_e32 v18, v27, v20
	v_sub_f32_e32 v10, v23, v10
	v_mul_f32_e32 v23, v28, v18
	v_fma_f32 v24, v18, v28, -v23
	v_fmac_f32_e32 v24, v18, v11
	v_add_f32_e32 v30, v23, v24
	v_sub_f32_e32 v31, v27, v30
	v_sub_f32_e32 v23, v30, v23
	v_sub_f32_e32 v27, v27, v31
	v_sub_f32_e32 v23, v23, v24
	v_sub_f32_e32 v24, v27, v30
	v_add_f32_e32 v10, v10, v24
	v_add_f32_e32 v10, v23, v10
	v_add_f32_e32 v23, v31, v10
	v_mul_f32_e32 v24, v20, v23
	v_sub_f32_e32 v27, v31, v23
	v_mul_f32_e32 v30, v28, v24
	v_add_f32_e32 v10, v10, v27
	v_add_f32_e32 v27, v18, v24
	v_fma_f32 v28, v24, v28, -v30
	v_sub_f32_e32 v18, v27, v18
	v_fmac_f32_e32 v28, v24, v11
	v_sub_f32_e32 v11, v24, v18
	v_add_f32_e32 v18, v30, v28
	v_sub_f32_e32 v24, v18, v30
	v_sub_f32_e32 v30, v23, v18
	v_sub_f32_e32 v23, v23, v30
	v_sub_f32_e32 v18, v23, v18
	v_sub_f32_e32 v24, v24, v28
	v_add_f32_e32 v10, v10, v18
	v_add_f32_e32 v10, v24, v10
	v_add_f32_e32 v10, v30, v10
	v_mul_f32_e32 v10, v20, v10
	v_add_f32_e32 v10, v11, v10
	v_add_f32_e32 v11, v27, v10
	v_mul_f32_e32 v18, v11, v11
	v_mov_b32_e32 v28, 0x3ecc95a3
	v_fmamk_f32 v24, v18, 0x3e9b6dac, v28
	v_sub_f32_e32 v20, v11, v27
	v_ldexp_f32 v23, v11, 1
	v_mul_f32_e32 v11, v11, v18
	v_fmaak_f32 v18, v18, v24, 0x3f2aaada
	v_mul_f32_e32 v11, v11, v18
	v_add_f32_e32 v18, v23, v11
	v_sub_f32_e32 v10, v10, v20
	v_sub_f32_e32 v20, v18, v23
	v_ldexp_f32 v10, v10, 1
	v_sub_f32_e32 v11, v11, v20
	v_add_f32_e32 v10, v10, v11
	v_add_f32_e32 v11, v18, v10
	v_sub_f32_e32 v18, v11, v18
	v_add_f32_e32 v20, v21, v11
	v_sub_f32_e32 v10, v10, v18
	v_sub_f32_e32 v18, v20, v21
	v_sub_f32_e32 v23, v20, v18
	v_sub_f32_e32 v11, v11, v18
	v_add_f32_e32 v18, v12, v10
	v_sub_f32_e32 v21, v21, v23
	v_sub_f32_e32 v23, v18, v12
	v_add_f32_e32 v11, v11, v21
	v_sub_f32_e32 v21, v18, v23
	v_sub_f32_e32 v10, v10, v23
	v_sub_f32_e32 v12, v12, v21
	v_add_f32_e32 v11, v18, v11
	v_add_f32_e32 v10, v10, v12
	v_add_f32_e32 v12, v20, v11
	v_sub_f32_e32 v18, v12, v20
	v_sub_f32_e32 v11, v11, v18
	v_add_f32_e32 v10, v10, v11
	v_add_f32_e32 v10, v12, v10
	v_cmp_neq_f32_e32 vcc, s23, v15
	v_add_f32_e32 v29, v25, v26
	s_waitcnt vmcnt(3)
	v_add_f32_e32 v7, v8, v7
	v_cndmask_b32_e32 v10, v219, v10, vcc
	v_cmp_ngt_f32_e32 vcc, -1.0, v15
	s_nop 1
	v_cndmask_b32_e32 v10, v220, v10, vcc
	v_cmp_neq_f32_e32 vcc, -1.0, v15
	s_nop 1
	v_cndmask_b32_e32 v10, v221, v10, vcc
	v_cmp_lt_f32_e64 vcc, |v15|, s6
	s_nop 1
	v_cndmask_b32_e32 v10, v10, v15, vcc
	v_add_f32_e32 v11, v1, v10
	v_sub_u32_e32 v1, 0, v13
	v_add_f32_e32 v13, -1.0, v19
	v_sub_f32_e32 v15, v16, v13
	v_sub_f32_e32 v13, v13, v19
	v_ldexp_f32 v10, v19, v1
	v_add_f32_e32 v13, 1.0, v13
	v_add_f32_e32 v13, v15, v13
	v_add_f32_e32 v15, 1.0, v10
	v_add_f32_e32 v18, -1.0, v15
	v_ldexp_f32 v1, v13, v1
	v_sub_f32_e32 v18, v10, v18
	v_add_f32_e32 v18, v1, v18
	v_add_f32_e32 v12, -1.0, v10
	v_add_f32_e32 v19, v15, v18
	v_add_f32_e32 v13, 1.0, v12
	v_rcp_f32_e32 v20, v19
	v_sub_f32_e32 v10, v10, v13
	v_add_f32_e32 v1, v1, v10
	v_add_f32_e32 v10, v12, v1
	v_mul_f32_e32 v13, v10, v20
	v_mul_f32_e32 v21, v19, v13
	v_sub_f32_e32 v15, v19, v15
	v_sub_f32_e32 v15, v18, v15
	v_fma_f32 v18, v13, v19, -v21
	v_fmac_f32_e32 v18, v13, v15
	v_add_f32_e32 v23, v21, v18
	v_sub_f32_e32 v24, v10, v23
	v_sub_f32_e32 v12, v10, v12
	v_sub_f32_e32 v10, v10, v24
	v_sub_f32_e32 v21, v23, v21
	v_sub_f32_e32 v1, v1, v12
	v_sub_f32_e32 v10, v10, v23
	v_sub_f32_e32 v18, v21, v18
	v_add_f32_e32 v1, v1, v10
	v_add_f32_e32 v1, v18, v1
	v_add_f32_e32 v10, v24, v1
	v_mul_f32_e32 v12, v20, v10
	v_mul_f32_e32 v21, v19, v12
	v_add_f32_e32 v18, v13, v12
	v_fma_f32 v19, v12, v19, -v21
	v_sub_f32_e32 v13, v18, v13
	v_fmac_f32_e32 v19, v12, v15
	v_sub_f32_e32 v13, v12, v13
	v_add_f32_e32 v12, v21, v19
	v_sub_f32_e32 v15, v10, v12
	v_sub_f32_e32 v21, v12, v21
	v_sub_f32_e32 v19, v21, v19
	v_sub_f32_e32 v21, v24, v10
	v_sub_f32_e32 v10, v10, v15
	v_add_f32_e32 v1, v1, v21
	v_sub_f32_e32 v10, v10, v12
	v_add_f32_e32 v1, v1, v10
	v_add_f32_e32 v1, v19, v1
	v_add_f32_e32 v1, v15, v1
	v_mul_f32_e32 v1, v20, v1
	v_add_f32_e32 v1, v13, v1
	v_add_f32_e32 v10, v18, v1
	v_mul_f32_e32 v13, v10, v10
	v_fmamk_f32 v19, v13, 0x3e9b6dac, v28
	v_mul_f32_e32 v15, v10, v13
	v_fmaak_f32 v13, v13, v19, 0x3f2aaada
	v_ldexp_f32 v12, v10, 1
	v_mul_f32_e32 v13, v15, v13
	v_add_f32_e32 v15, v12, v13
	v_sub_f32_e32 v10, v10, v18
	v_sub_f32_e32 v1, v1, v10
	v_sub_f32_e32 v10, v15, v12
	v_ldexp_f32 v1, v1, 1
	v_sub_f32_e32 v10, v13, v10
	v_add_f32_e32 v1, v1, v10
	v_add_f32_e32 v10, v15, v1
	v_add_f32_e32 v12, v29, v10
	v_sub_f32_e32 v18, v12, v29
	v_sub_f32_e32 v13, v29, v25
	v_sub_f32_e32 v15, v10, v15
	v_sub_f32_e32 v10, v10, v18
	v_sub_f32_e32 v18, v12, v18
	v_sub_f32_e32 v13, v26, v13
	v_sub_f32_e32 v1, v1, v15
	v_sub_f32_e32 v18, v29, v18
	v_add_f32_e32 v15, v13, v1
	v_add_f32_e32 v10, v10, v18
	v_add_f32_e32 v10, v15, v10
	v_sub_f32_e32 v19, v15, v13
	v_add_f32_e32 v18, v12, v10
	v_sub_f32_e32 v15, v15, v19
	v_sub_f32_e32 v1, v1, v19
	v_sub_f32_e32 v13, v13, v15
	v_sub_f32_e32 v12, v18, v12
	v_add_f32_e32 v1, v1, v13
	v_sub_f32_e32 v10, v10, v12
	v_add_f32_e32 v1, v1, v10
	s_waitcnt vmcnt(0)
	v_add_f32_e32 v10, v8, v14
	v_mul_f32_e64 v12, |v10|, s22
	v_exp_f32_e32 v14, v12
	v_add_f32_e32 v1, v18, v1
	v_cmp_neq_f32_e32 vcc, s23, v16
	v_max_f32_e64 v10, -v10, 0
	v_add_f32_e32 v15, 1.0, v14
	v_cndmask_b32_e32 v1, v219, v1, vcc
	v_cmp_ngt_f32_e32 vcc, -1.0, v16
	v_cvt_f64_f32_e32 v[12:13], v15
	v_frexp_exp_i32_f64_e32 v12, v[12:13]
	v_cndmask_b32_e32 v1, v220, v1, vcc
	v_cmp_neq_f32_e32 vcc, -1.0, v16
	v_frexp_mant_f32_e32 v13, v15
	v_add_f32_e32 v20, -1.0, v15
	v_cndmask_b32_e32 v1, v221, v1, vcc
	v_cmp_lt_f32_e64 vcc, |v16|, s6
	v_sub_f32_e32 v21, v14, v20
	s_nop 0
	v_cndmask_b32_e32 v1, v1, v16, vcc
	v_cmp_gt_f32_e32 vcc, s0, v13
	v_add_f32_e32 v1, v17, v1
	v_sub_f32_e64 v1, -v11, v1
	v_subbrev_co_u32_e32 v12, vcc, 0, v12, vcc
	v_cvt_f32_i32_e32 v13, v12
	v_sub_u32_e32 v12, 0, v12
	v_ldexp_f32 v18, v15, v12
	v_sub_f32_e32 v15, v20, v15
	v_add_f32_e32 v15, 1.0, v15
	v_add_f32_e32 v20, 1.0, v18
	v_add_f32_e32 v15, v21, v15
	v_add_f32_e32 v21, -1.0, v20
	v_ldexp_f32 v12, v15, v12
	v_sub_f32_e32 v21, v18, v21
	v_add_f32_e32 v21, v12, v21
	v_add_f32_e32 v19, -1.0, v18
	v_add_f32_e32 v23, v20, v21
	v_add_f32_e32 v15, 1.0, v19
	v_rcp_f32_e32 v24, v23
	v_sub_f32_e32 v15, v18, v15
	v_add_f32_e32 v12, v12, v15
	v_add_f32_e32 v15, v19, v12
	v_mul_f32_e32 v18, v15, v24
	v_mul_f32_e32 v25, v23, v18
	v_sub_f32_e32 v20, v23, v20
	v_sub_f32_e32 v20, v21, v20
	v_fma_f32 v21, v18, v23, -v25
	v_fmac_f32_e32 v21, v18, v20
	v_add_f32_e32 v26, v25, v21
	v_sub_f32_e32 v27, v15, v26
	v_sub_f32_e32 v19, v15, v19
	v_sub_f32_e32 v15, v15, v27
	v_sub_f32_e32 v25, v26, v25
	v_sub_f32_e32 v12, v12, v19
	v_sub_f32_e32 v15, v15, v26
	v_sub_f32_e32 v21, v25, v21
	v_add_f32_e32 v12, v12, v15
	v_add_f32_e32 v12, v21, v12
	v_add_f32_e32 v15, v27, v12
	v_mul_f32_e32 v19, v24, v15
	v_mul_f32_e32 v25, v23, v19
	v_add_f32_e32 v21, v18, v19
	v_fma_f32 v23, v19, v23, -v25
	v_sub_f32_e32 v18, v21, v18
	v_fmac_f32_e32 v23, v19, v20
	v_sub_f32_e32 v18, v19, v18
	v_add_f32_e32 v19, v25, v23
	v_sub_f32_e32 v20, v15, v19
	v_sub_f32_e32 v25, v19, v25
	v_sub_f32_e32 v23, v25, v23
	v_sub_f32_e32 v25, v27, v15
	v_sub_f32_e32 v15, v15, v20
	v_add_f32_e32 v12, v12, v25
	v_sub_f32_e32 v15, v15, v19
	v_add_f32_e32 v12, v12, v15
	v_add_f32_e32 v12, v23, v12
	v_add_f32_e32 v12, v20, v12
	v_mul_f32_e32 v12, v24, v12
	v_add_f32_e32 v12, v18, v12
	v_add_f32_e32 v15, v21, v12
	v_mul_f32_e32 v19, v15, v15
	v_fmamk_f32 v23, v19, 0x3e9b6dac, v28
	v_mul_f32_e32 v20, v15, v19
	v_fmaak_f32 v19, v19, v23, 0x3f2aaada
	v_ldexp_f32 v18, v15, 1
	v_mul_f32_e32 v19, v20, v19
	v_add_f32_e32 v20, v18, v19
	v_sub_f32_e32 v15, v15, v21
	v_mul_f32_e32 v16, 0x3f317218, v13
	v_sub_f32_e32 v12, v12, v15
	v_sub_f32_e32 v15, v20, v18
	v_fma_f32 v17, v13, s1, -v16
	v_ldexp_f32 v12, v12, 1
	v_sub_f32_e32 v15, v19, v15
	v_fmac_f32_e32 v17, 0xb102e308, v13
	v_add_f32_e32 v12, v12, v15
	v_add_f32_e32 v13, v16, v17
	v_add_f32_e32 v15, v20, v12
	v_add_f32_e32 v18, v13, v15
	v_sub_f32_e32 v16, v13, v16
	v_sub_f32_e32 v16, v17, v16
	v_sub_f32_e32 v17, v15, v20
	v_sub_f32_e32 v19, v18, v13
	v_sub_f32_e32 v12, v12, v17
	v_sub_f32_e32 v15, v15, v19
	v_sub_f32_e32 v19, v18, v19
	v_add_f32_e32 v17, v16, v12
	v_sub_f32_e32 v13, v13, v19
	v_add_f32_e32 v13, v15, v13
	v_sub_f32_e32 v19, v17, v16
	v_add_f32_e32 v13, v17, v13
	v_sub_f32_e32 v17, v17, v19
	v_add_f32_e32 v15, v18, v13
	v_sub_f32_e32 v12, v12, v19
	v_sub_f32_e32 v16, v16, v17
	v_add_f32_e32 v12, v12, v16
	v_sub_f32_e32 v16, v15, v18
	v_sub_f32_e32 v13, v13, v16
	v_add_f32_e32 v12, v12, v13
	v_mul_f32_e64 v13, |v5|, s22
	v_add_f32_e32 v12, v15, v12
	v_exp_f32_e32 v15, v13
	v_cmp_neq_f32_e32 vcc, s23, v14
	v_max_f32_e64 v5, -v5, 0
	v_add_f32_e32 v17, 1.0, v15
	v_cndmask_b32_e32 v12, v219, v12, vcc
	v_cmp_ngt_f32_e32 vcc, -1.0, v14
	v_add_f32_e32 v20, -1.0, v17
	v_sub_f32_e32 v21, v15, v20
	v_cndmask_b32_e32 v12, v220, v12, vcc
	v_cmp_neq_f32_e32 vcc, -1.0, v14
	s_nop 1
	v_cndmask_b32_e32 v16, v221, v12, vcc
	v_cvt_f64_f32_e32 v[12:13], v17
	v_frexp_exp_i32_f64_e32 v12, v[12:13]
	v_frexp_mant_f32_e32 v13, v17
	v_cmp_gt_f32_e32 vcc, s0, v13
	s_nop 1
	v_subbrev_co_u32_e32 v12, vcc, 0, v12, vcc
	v_cvt_f32_i32_e32 v13, v12
	v_sub_u32_e32 v12, 0, v12
	v_ldexp_f32 v18, v17, v12
	v_sub_f32_e32 v17, v20, v17
	v_add_f32_e32 v17, 1.0, v17
	v_add_f32_e32 v20, 1.0, v18
	v_add_f32_e32 v17, v21, v17
	v_add_f32_e32 v21, -1.0, v20
	v_ldexp_f32 v12, v17, v12
	v_sub_f32_e32 v21, v18, v21
	v_add_f32_e32 v21, v12, v21
	v_add_f32_e32 v19, -1.0, v18
	v_add_f32_e32 v23, v20, v21
	v_add_f32_e32 v17, 1.0, v19
	v_rcp_f32_e32 v24, v23
	v_sub_f32_e32 v17, v18, v17
	v_add_f32_e32 v12, v12, v17
	v_add_f32_e32 v17, v19, v12
	v_mul_f32_e32 v18, v17, v24
	v_mul_f32_e32 v25, v23, v18
	v_sub_f32_e32 v20, v23, v20
	v_sub_f32_e32 v20, v21, v20
	v_fma_f32 v21, v18, v23, -v25
	v_fmac_f32_e32 v21, v18, v20
	v_add_f32_e32 v26, v25, v21
	v_sub_f32_e32 v27, v17, v26
	v_sub_f32_e32 v19, v17, v19
	v_sub_f32_e32 v17, v17, v27
	v_sub_f32_e32 v25, v26, v25
	v_sub_f32_e32 v12, v12, v19
	v_sub_f32_e32 v17, v17, v26
	v_sub_f32_e32 v21, v25, v21
	v_add_f32_e32 v12, v12, v17
	v_add_f32_e32 v12, v21, v12
	v_add_f32_e32 v17, v27, v12
	v_mul_f32_e32 v19, v24, v17
	v_mul_f32_e32 v25, v23, v19
	v_add_f32_e32 v21, v18, v19
	v_fma_f32 v23, v19, v23, -v25
	v_sub_f32_e32 v18, v21, v18
	v_fmac_f32_e32 v23, v19, v20
	v_sub_f32_e32 v18, v19, v18
	v_add_f32_e32 v19, v25, v23
	v_sub_f32_e32 v20, v17, v19
	v_sub_f32_e32 v25, v19, v25
	v_sub_f32_e32 v23, v25, v23
	v_sub_f32_e32 v25, v27, v17
	v_sub_f32_e32 v17, v17, v20
	v_add_f32_e32 v12, v12, v25
	v_sub_f32_e32 v17, v17, v19
	v_add_f32_e32 v12, v12, v17
	v_add_f32_e32 v12, v23, v12
	v_add_f32_e32 v12, v20, v12
	v_mul_f32_e32 v12, v24, v12
	v_add_f32_e32 v12, v18, v12
	v_add_f32_e32 v17, v21, v12
	v_mul_f32_e32 v19, v17, v17
	v_fmamk_f32 v23, v19, 0x3e9b6dac, v28
	v_mul_f32_e32 v20, v17, v19
	v_fmaak_f32 v19, v19, v23, 0x3f2aaada
	v_cmp_lt_f32_e64 vcc, |v14|, s6
	v_ldexp_f32 v18, v17, 1
	v_mul_f32_e32 v19, v20, v19
	v_cndmask_b32_e32 v14, v16, v14, vcc
	v_add_f32_e32 v20, v18, v19
	v_sub_f32_e32 v17, v17, v21
	v_add_f32_e32 v10, v10, v14
	v_mul_f32_e32 v14, 0x3f317218, v13
	v_sub_f32_e32 v12, v12, v17
	v_sub_f32_e32 v17, v20, v18
	v_fma_f32 v16, v13, s1, -v14
	v_ldexp_f32 v12, v12, 1
	v_sub_f32_e32 v17, v19, v17
	v_fmac_f32_e32 v16, 0xb102e308, v13
	v_add_f32_e32 v12, v12, v17
	v_add_f32_e32 v13, v14, v16
	v_add_f32_e32 v17, v20, v12
	v_add_f32_e32 v18, v13, v17
	v_sub_f32_e32 v14, v13, v14
	v_sub_f32_e32 v14, v16, v14
	v_sub_f32_e32 v16, v17, v20
	v_sub_f32_e32 v19, v18, v13
	v_sub_f32_e32 v12, v12, v16
	v_sub_f32_e32 v17, v17, v19
	v_sub_f32_e32 v19, v18, v19
	v_add_f32_e32 v16, v14, v12
	v_sub_f32_e32 v13, v13, v19
	v_add_f32_e32 v13, v17, v13
	v_sub_f32_e32 v19, v16, v14
	v_add_f32_e32 v13, v16, v13
	v_sub_f32_e32 v16, v16, v19
	v_add_f32_e32 v17, v18, v13
	v_sub_f32_e32 v12, v12, v19
	v_sub_f32_e32 v14, v14, v16
	v_add_f32_e32 v12, v12, v14
	v_sub_f32_e32 v14, v17, v18
	v_sub_f32_e32 v13, v13, v14
	v_add_f32_e32 v12, v12, v13
	v_add_f32_e32 v13, v8, v4
	v_mul_f32_e64 v4, |v13|, s22
	v_add_f32_e32 v12, v17, v12
	v_cmp_neq_f32_e32 vcc, s23, v15
	v_exp_f32_e32 v14, v4
	s_nop 0
	v_cndmask_b32_e32 v12, v219, v12, vcc
	v_cmp_ngt_f32_e32 vcc, -1.0, v15
	s_nop 1
	v_cndmask_b32_e32 v12, v220, v12, vcc
	v_cmp_neq_f32_e32 vcc, -1.0, v15
	s_nop 1
	v_cndmask_b32_e32 v12, v221, v12, vcc
	v_cmp_lt_f32_e64 vcc, |v15|, s6
	s_nop 1
	v_cndmask_b32_e32 v4, v12, v15, vcc
	v_add_f32_e32 v15, 1.0, v14
	v_add_f32_e32 v12, v5, v4
	v_cvt_f64_f32_e32 v[4:5], v15
	v_frexp_exp_i32_f64_e32 v4, v[4:5]
	v_frexp_mant_f32_e32 v5, v15
	v_cmp_gt_f32_e32 vcc, s0, v5
	v_add_f32_e32 v20, -1.0, v15
	v_sub_f32_e32 v21, v14, v20
	v_subbrev_co_u32_e32 v16, vcc, 0, v4, vcc
	v_cvt_f32_i32_e32 v17, v16
	v_sub_u32_e32 v16, 0, v16
	v_ldexp_f32 v18, v15, v16
	v_sub_f32_e32 v15, v20, v15
	v_add_f32_e32 v15, 1.0, v15
	v_add_f32_e32 v20, 1.0, v18
	v_add_f32_e32 v15, v21, v15
	v_add_f32_e32 v21, -1.0, v20
	v_ldexp_f32 v15, v15, v16
	v_sub_f32_e32 v21, v18, v21
	v_add_f32_e32 v21, v15, v21
	v_add_f32_e32 v19, -1.0, v18
	v_add_f32_e32 v23, v20, v21
	v_add_f32_e32 v16, 1.0, v19
	v_rcp_f32_e32 v24, v23
	v_sub_f32_e32 v16, v18, v16
	v_add_f32_e32 v15, v15, v16
	v_add_f32_e32 v16, v19, v15
	v_mul_f32_e32 v18, v16, v24
	v_mul_f32_e32 v25, v23, v18
	v_sub_f32_e32 v20, v23, v20
	v_sub_f32_e32 v20, v21, v20
	v_fma_f32 v21, v18, v23, -v25
	v_fmac_f32_e32 v21, v18, v20
	v_add_f32_e32 v26, v25, v21
	v_sub_f32_e32 v27, v16, v26
	v_sub_f32_e32 v19, v16, v19
	v_sub_f32_e32 v16, v16, v27
	v_sub_f32_e32 v25, v26, v25
	v_sub_f32_e32 v15, v15, v19
	v_sub_f32_e32 v16, v16, v26
	v_sub_f32_e32 v21, v25, v21
	v_add_f32_e32 v15, v15, v16
	v_add_f32_e32 v15, v21, v15
	v_add_f32_e32 v16, v27, v15
	v_mul_f32_e32 v19, v24, v16
	v_mul_f32_e32 v25, v23, v19
	v_add_f32_e32 v21, v18, v19
	v_fma_f32 v23, v19, v23, -v25
	v_sub_f32_e32 v18, v21, v18
	v_fmac_f32_e32 v23, v19, v20
	v_sub_f32_e32 v18, v19, v18
	v_add_f32_e32 v19, v25, v23
	v_sub_f32_e32 v20, v16, v19
	v_sub_f32_e32 v25, v19, v25
	v_sub_f32_e32 v23, v25, v23
	v_sub_f32_e32 v25, v27, v16
	v_sub_f32_e32 v16, v16, v20
	v_add_f32_e32 v15, v15, v25
	v_sub_f32_e32 v16, v16, v19
	v_add_f32_e32 v15, v15, v16
	v_add_f32_e32 v15, v23, v15
	v_add_f32_e32 v15, v20, v15
	v_mul_f32_e32 v15, v24, v15
	v_add_f32_e32 v15, v18, v15
	v_add_f32_e32 v16, v21, v15
	v_mul_f32_e32 v19, v16, v16
	v_fmamk_f32 v23, v19, 0x3e9b6dac, v28
	v_mul_f32_e32 v20, v16, v19
	v_fmaak_f32 v19, v19, v23, 0x3f2aaada
	v_ldexp_f32 v18, v16, 1
	v_mul_f32_e32 v19, v20, v19
	v_sub_f32_e32 v4, v1, v10
	v_add_f32_e32 v20, v18, v19
	v_sub_f32_e32 v16, v16, v21
	v_sub_f32_e32 v5, v4, v12
	v_mul_f32_e32 v12, 0x3f317218, v17
	v_sub_f32_e32 v15, v15, v16
	v_sub_f32_e32 v16, v20, v18
	v_max_f32_e64 v10, -v13, 0
	v_fma_f32 v13, v17, s1, -v12
	v_ldexp_f32 v15, v15, 1
	v_sub_f32_e32 v16, v19, v16
	v_fmac_f32_e32 v13, 0xb102e308, v17
	v_add_f32_e32 v15, v15, v16
	v_add_f32_e32 v17, v12, v13
	v_add_f32_e32 v16, v20, v15
	v_add_f32_e32 v18, v17, v16
	v_sub_f32_e32 v12, v17, v12
	v_sub_f32_e32 v12, v13, v12
	v_sub_f32_e32 v13, v16, v20
	v_sub_f32_e32 v19, v18, v17
	v_sub_f32_e32 v13, v15, v13
	v_sub_f32_e32 v16, v16, v19
	v_sub_f32_e32 v19, v18, v19
	v_add_f32_e32 v15, v12, v13
	v_sub_f32_e32 v17, v17, v19
	v_add_f32_e32 v16, v16, v17
	v_sub_f32_e32 v19, v15, v12
	v_add_f32_e32 v16, v15, v16
	v_sub_f32_e32 v15, v15, v19
	v_add_f32_e32 v17, v18, v16
	v_sub_f32_e32 v13, v13, v19
	v_sub_f32_e32 v12, v12, v15
	v_add_f32_e32 v12, v13, v12
	v_sub_f32_e32 v13, v17, v18
	v_sub_f32_e32 v13, v16, v13
	v_add_f32_e32 v12, v12, v13
	v_mul_f32_e64 v13, |v7|, s22
	v_exp_f32_e32 v15, v13
	v_add_f32_e32 v12, v17, v12
	v_cmp_neq_f32_e32 vcc, s23, v14
	v_max_f32_e64 v7, -v7, 0
	v_add_f32_e32 v17, 1.0, v15
	v_cndmask_b32_e32 v12, v219, v12, vcc
	v_cmp_ngt_f32_e32 vcc, -1.0, v14
	v_add_f32_e32 v20, -1.0, v17
	v_sub_f32_e32 v21, v15, v20
	v_cndmask_b32_e32 v12, v220, v12, vcc
	v_cmp_neq_f32_e32 vcc, -1.0, v14
	s_nop 1
	v_cndmask_b32_e32 v16, v221, v12, vcc
	v_cvt_f64_f32_e32 v[12:13], v17
	v_frexp_exp_i32_f64_e32 v12, v[12:13]
	v_frexp_mant_f32_e32 v13, v17
	v_cmp_gt_f32_e32 vcc, s0, v13
	s_nop 1
	v_subbrev_co_u32_e32 v12, vcc, 0, v12, vcc
	v_cvt_f32_i32_e32 v13, v12
	v_sub_u32_e32 v12, 0, v12
	v_ldexp_f32 v18, v17, v12
	v_sub_f32_e32 v17, v20, v17
	v_add_f32_e32 v17, 1.0, v17
	v_add_f32_e32 v20, 1.0, v18
	v_add_f32_e32 v17, v21, v17
	v_add_f32_e32 v21, -1.0, v20
	v_ldexp_f32 v12, v17, v12
	v_sub_f32_e32 v21, v18, v21
	v_add_f32_e32 v21, v12, v21
	v_add_f32_e32 v19, -1.0, v18
	v_add_f32_e32 v23, v20, v21
	v_add_f32_e32 v17, 1.0, v19
	v_rcp_f32_e32 v24, v23
	v_sub_f32_e32 v17, v18, v17
	v_add_f32_e32 v12, v12, v17
	v_add_f32_e32 v17, v19, v12
	v_mul_f32_e32 v18, v17, v24
	v_mul_f32_e32 v25, v23, v18
	v_sub_f32_e32 v20, v23, v20
	v_sub_f32_e32 v20, v21, v20
	v_fma_f32 v21, v18, v23, -v25
	v_fmac_f32_e32 v21, v18, v20
	v_add_f32_e32 v26, v25, v21
	v_sub_f32_e32 v27, v17, v26
	v_sub_f32_e32 v19, v17, v19
	v_sub_f32_e32 v17, v17, v27
	v_sub_f32_e32 v25, v26, v25
	v_sub_f32_e32 v12, v12, v19
	v_sub_f32_e32 v17, v17, v26
	v_sub_f32_e32 v21, v25, v21
	v_add_f32_e32 v12, v12, v17
	v_add_f32_e32 v12, v21, v12
	v_add_f32_e32 v17, v27, v12
	v_mul_f32_e32 v19, v24, v17
	v_mul_f32_e32 v25, v23, v19
	v_add_f32_e32 v21, v18, v19
	v_fma_f32 v23, v19, v23, -v25
	v_sub_f32_e32 v18, v21, v18
	v_fmac_f32_e32 v23, v19, v20
	v_sub_f32_e32 v18, v19, v18
	v_add_f32_e32 v19, v25, v23
	v_sub_f32_e32 v20, v17, v19
	v_sub_f32_e32 v25, v19, v25
	v_sub_f32_e32 v23, v25, v23
	v_sub_f32_e32 v25, v27, v17
	v_sub_f32_e32 v17, v17, v20
	v_add_f32_e32 v12, v12, v25
	v_sub_f32_e32 v17, v17, v19
	v_add_f32_e32 v12, v12, v17
	v_add_f32_e32 v12, v23, v12
	v_add_f32_e32 v12, v20, v12
	v_mul_f32_e32 v12, v24, v12
	v_add_f32_e32 v12, v18, v12
	v_add_f32_e32 v17, v21, v12
	v_mul_f32_e32 v19, v17, v17
	v_fmamk_f32 v23, v19, 0x3e9b6dac, v28
	v_mul_f32_e32 v20, v17, v19
	v_fmaak_f32 v19, v19, v23, 0x3f2aaada
	v_cmp_lt_f32_e64 vcc, |v14|, s6
	v_ldexp_f32 v18, v17, 1
	v_mul_f32_e32 v19, v20, v19
	v_cndmask_b32_e32 v14, v16, v14, vcc
	v_add_f32_e32 v20, v18, v19
	v_sub_f32_e32 v17, v17, v21
	v_add_f32_e32 v10, v10, v14
	v_mul_f32_e32 v14, 0x3f317218, v13
	v_sub_f32_e32 v12, v12, v17
	v_sub_f32_e32 v17, v20, v18
	v_fma_f32 v16, v13, s1, -v14
	v_ldexp_f32 v12, v12, 1
	v_sub_f32_e32 v17, v19, v17
	v_fmac_f32_e32 v16, 0xb102e308, v13
	v_add_f32_e32 v12, v12, v17
	v_add_f32_e32 v13, v14, v16
	v_add_f32_e32 v17, v20, v12
	v_add_f32_e32 v18, v13, v17
	v_sub_f32_e32 v14, v13, v14
	v_sub_f32_e32 v14, v16, v14
	v_sub_f32_e32 v16, v17, v20
	v_sub_f32_e32 v19, v18, v13
	v_sub_f32_e32 v12, v12, v16
	v_sub_f32_e32 v17, v17, v19
	v_sub_f32_e32 v19, v18, v19
	v_add_f32_e32 v16, v14, v12
	v_sub_f32_e32 v13, v13, v19
	v_add_f32_e32 v13, v17, v13
	v_sub_f32_e32 v19, v16, v14
	v_add_f32_e32 v13, v16, v13
	v_sub_f32_e32 v16, v16, v19
	v_add_f32_e32 v17, v18, v13
	v_sub_f32_e32 v12, v12, v19
	v_sub_f32_e32 v14, v14, v16
	v_add_f32_e32 v12, v12, v14
	v_sub_f32_e32 v14, v17, v18
	v_sub_f32_e32 v13, v13, v14
	v_add_f32_e32 v12, v12, v13
	v_add_f32_e32 v13, v8, v6
	v_mul_f32_e64 v6, |v13|, s22
	v_add_f32_e32 v12, v17, v12
	v_cmp_neq_f32_e32 vcc, s23, v15
	v_exp_f32_e32 v14, v6
	s_nop 0
	v_cndmask_b32_e32 v12, v219, v12, vcc
	v_cmp_ngt_f32_e32 vcc, -1.0, v15
	s_nop 1
	v_cndmask_b32_e32 v12, v220, v12, vcc
	v_cmp_neq_f32_e32 vcc, -1.0, v15
	s_nop 1
	v_cndmask_b32_e32 v12, v221, v12, vcc
	v_cmp_lt_f32_e64 vcc, |v15|, s6
	s_nop 1
	v_cndmask_b32_e32 v6, v12, v15, vcc
	v_add_f32_e32 v15, 1.0, v14
	v_add_f32_e32 v12, v7, v6
	v_cvt_f64_f32_e32 v[6:7], v15
	v_frexp_exp_i32_f64_e32 v6, v[6:7]
	v_frexp_mant_f32_e32 v7, v15
	v_cmp_gt_f32_e32 vcc, s0, v7
	v_add_f32_e32 v20, -1.0, v15
	v_sub_f32_e32 v21, v14, v20
	v_subbrev_co_u32_e32 v16, vcc, 0, v6, vcc
	v_cvt_f32_i32_e32 v17, v16
	v_sub_u32_e32 v16, 0, v16
	v_ldexp_f32 v18, v15, v16
	v_sub_f32_e32 v15, v20, v15
	v_add_f32_e32 v15, 1.0, v15
	v_add_f32_e32 v20, 1.0, v18
	v_add_f32_e32 v15, v21, v15
	v_add_f32_e32 v21, -1.0, v20
	v_ldexp_f32 v15, v15, v16
	v_sub_f32_e32 v21, v18, v21
	v_add_f32_e32 v21, v15, v21
	v_add_f32_e32 v19, -1.0, v18
	v_add_f32_e32 v23, v20, v21
	v_add_f32_e32 v16, 1.0, v19
	v_rcp_f32_e32 v24, v23
	v_sub_f32_e32 v16, v18, v16
	v_add_f32_e32 v15, v15, v16
	v_add_f32_e32 v16, v19, v15
	v_mul_f32_e32 v18, v16, v24
	v_mul_f32_e32 v25, v23, v18
	v_sub_f32_e32 v20, v23, v20
	v_sub_f32_e32 v20, v21, v20
	v_fma_f32 v21, v18, v23, -v25
	v_fmac_f32_e32 v21, v18, v20
	v_add_f32_e32 v26, v25, v21
	v_sub_f32_e32 v27, v16, v26
	v_sub_f32_e32 v19, v16, v19
	v_sub_f32_e32 v16, v16, v27
	v_sub_f32_e32 v25, v26, v25
	v_sub_f32_e32 v15, v15, v19
	v_sub_f32_e32 v16, v16, v26
	v_sub_f32_e32 v21, v25, v21
	v_add_f32_e32 v15, v15, v16
	v_add_f32_e32 v15, v21, v15
	v_add_f32_e32 v16, v27, v15
	v_mul_f32_e32 v19, v24, v16
	v_mul_f32_e32 v25, v23, v19
	v_add_f32_e32 v21, v18, v19
	v_fma_f32 v23, v19, v23, -v25
	v_sub_f32_e32 v18, v21, v18
	v_fmac_f32_e32 v23, v19, v20
	v_sub_f32_e32 v18, v19, v18
	v_add_f32_e32 v19, v25, v23
	v_sub_f32_e32 v20, v16, v19
	v_sub_f32_e32 v25, v19, v25
	v_sub_f32_e32 v23, v25, v23
	v_sub_f32_e32 v25, v27, v16
	v_sub_f32_e32 v16, v16, v20
	v_add_f32_e32 v15, v15, v25
	v_sub_f32_e32 v16, v16, v19
	v_add_f32_e32 v15, v15, v16
	v_add_f32_e32 v15, v23, v15
	v_add_f32_e32 v15, v20, v15
	v_mul_f32_e32 v15, v24, v15
	v_add_f32_e32 v15, v18, v15
	v_add_f32_e32 v16, v21, v15
	v_mul_f32_e32 v19, v16, v16
	v_fmamk_f32 v23, v19, 0x3e9b6dac, v28
	v_mul_f32_e32 v20, v16, v19
	v_fmaak_f32 v19, v19, v23, 0x3f2aaada
	v_ldexp_f32 v18, v16, 1
	v_mul_f32_e32 v19, v20, v19
	v_sub_f32_e32 v6, v5, v10
	v_add_f32_e32 v20, v18, v19
	v_sub_f32_e32 v16, v16, v21
	v_sub_f32_e32 v7, v6, v12
	v_mul_f32_e32 v12, 0x3f317218, v17
	v_sub_f32_e32 v15, v15, v16
	v_sub_f32_e32 v16, v20, v18
	v_max_f32_e64 v10, -v13, 0
	v_fma_f32 v13, v17, s1, -v12
	v_ldexp_f32 v15, v15, 1
	v_sub_f32_e32 v16, v19, v16
	v_fmac_f32_e32 v13, 0xb102e308, v17
	v_add_f32_e32 v15, v15, v16
	v_add_f32_e32 v17, v12, v13
	v_add_f32_e32 v16, v20, v15
	v_add_f32_e32 v18, v17, v16
	v_sub_f32_e32 v12, v17, v12
	v_sub_f32_e32 v12, v13, v12
	v_sub_f32_e32 v13, v16, v20
	v_sub_f32_e32 v19, v18, v17
	v_sub_f32_e32 v13, v15, v13
	v_sub_f32_e32 v16, v16, v19
	v_sub_f32_e32 v19, v18, v19
	v_add_f32_e32 v15, v12, v13
	v_sub_f32_e32 v17, v17, v19
	v_add_f32_e32 v16, v16, v17
	v_sub_f32_e32 v19, v15, v12
	v_add_f32_e32 v16, v15, v16
	v_sub_f32_e32 v15, v15, v19
	v_add_f32_e32 v17, v18, v16
	v_sub_f32_e32 v13, v13, v19
	v_sub_f32_e32 v12, v12, v15
	v_add_f32_e32 v12, v13, v12
	v_sub_f32_e32 v13, v17, v18
	v_sub_f32_e32 v13, v16, v13
	v_add_f32_e32 v12, v12, v13
	v_add_f32_e32 v13, v8, v9
	v_mul_f32_e64 v8, |v13|, s22
	v_exp_f32_e32 v15, v8
	v_add_f32_e32 v12, v17, v12
	v_cmp_neq_f32_e32 vcc, s23, v14
	v_add_f32_e32 v16, 1.0, v15
	s_nop 0
	v_cndmask_b32_e32 v12, v219, v12, vcc
	v_cmp_ngt_f32_e32 vcc, -1.0, v14
	v_add_f32_e32 v19, -1.0, v16
	v_sub_f32_e32 v20, v15, v19
	v_cndmask_b32_e32 v8, v220, v12, vcc
	v_cmp_neq_f32_e32 vcc, -1.0, v14
	s_nop 1
	v_cndmask_b32_e32 v12, v221, v8, vcc
	v_cvt_f64_f32_e32 v[8:9], v16
	v_frexp_exp_i32_f64_e32 v8, v[8:9]
	v_frexp_mant_f32_e32 v9, v16
	v_cmp_gt_f32_e32 vcc, s0, v9
	s_nop 1
	v_subbrev_co_u32_e32 v8, vcc, 0, v8, vcc
	v_cvt_f32_i32_e32 v9, v8
	v_sub_u32_e32 v8, 0, v8
	v_ldexp_f32 v17, v16, v8
	v_sub_f32_e32 v16, v19, v16
	v_add_f32_e32 v16, 1.0, v16
	v_add_f32_e32 v19, 1.0, v17
	v_add_f32_e32 v16, v20, v16
	v_add_f32_e32 v20, -1.0, v19
	v_ldexp_f32 v8, v16, v8
	v_sub_f32_e32 v20, v17, v20
	v_add_f32_e32 v20, v8, v20
	v_add_f32_e32 v18, -1.0, v17
	v_add_f32_e32 v21, v19, v20
	v_add_f32_e32 v16, 1.0, v18
	v_rcp_f32_e32 v23, v21
	v_sub_f32_e32 v16, v17, v16
	v_add_f32_e32 v8, v8, v16
	v_add_f32_e32 v16, v18, v8
	v_mul_f32_e32 v17, v16, v23
	v_mul_f32_e32 v24, v21, v17
	v_sub_f32_e32 v19, v21, v19
	v_sub_f32_e32 v19, v20, v19
	v_fma_f32 v20, v17, v21, -v24
	v_fmac_f32_e32 v20, v17, v19
	v_add_f32_e32 v25, v24, v20
	v_sub_f32_e32 v26, v16, v25
	v_sub_f32_e32 v18, v16, v18
	v_sub_f32_e32 v16, v16, v26
	v_sub_f32_e32 v24, v25, v24
	v_sub_f32_e32 v8, v8, v18
	v_sub_f32_e32 v16, v16, v25
	v_sub_f32_e32 v20, v24, v20
	v_add_f32_e32 v8, v8, v16
	v_add_f32_e32 v8, v20, v8
	v_add_f32_e32 v16, v26, v8
	v_mul_f32_e32 v18, v23, v16
	v_mul_f32_e32 v24, v21, v18
	v_add_f32_e32 v20, v17, v18
	v_fma_f32 v21, v18, v21, -v24
	v_sub_f32_e32 v17, v20, v17
	v_fmac_f32_e32 v21, v18, v19
	v_sub_f32_e32 v17, v18, v17
	v_add_f32_e32 v18, v24, v21
	v_sub_f32_e32 v19, v16, v18
	v_sub_f32_e32 v24, v18, v24
	v_sub_f32_e32 v21, v24, v21
	v_sub_f32_e32 v24, v26, v16
	v_sub_f32_e32 v16, v16, v19
	v_add_f32_e32 v8, v8, v24
	v_sub_f32_e32 v16, v16, v18
	v_add_f32_e32 v8, v8, v16
	v_add_f32_e32 v8, v21, v8
	v_add_f32_e32 v8, v19, v8
	v_mul_f32_e32 v8, v23, v8
	v_add_f32_e32 v8, v17, v8
	v_add_f32_e32 v16, v20, v8
	v_mul_f32_e32 v18, v16, v16
	v_fmamk_f32 v21, v18, 0x3e9b6dac, v28
	v_mul_f32_e32 v19, v16, v18
	v_fmaak_f32 v18, v18, v21, 0x3f2aaada
	v_cmp_lt_f32_e64 vcc, |v14|, s6
	v_ldexp_f32 v17, v16, 1
	v_mul_f32_e32 v18, v19, v18
	v_cndmask_b32_e32 v12, v12, v14, vcc
	v_add_f32_e32 v19, v17, v18
	v_sub_f32_e32 v16, v16, v20
	v_add_f32_e32 v10, v10, v12
	v_max_f32_e64 v12, -v13, 0
	v_mul_f32_e32 v13, 0x3f317218, v9
	v_sub_f32_e32 v8, v8, v16
	v_sub_f32_e32 v16, v19, v17
	v_fma_f32 v14, v9, s1, -v13
	v_ldexp_f32 v8, v8, 1
	v_sub_f32_e32 v16, v18, v16
	v_fmac_f32_e32 v14, 0xb102e308, v9
	v_add_f32_e32 v8, v8, v16
	v_add_f32_e32 v9, v13, v14
	v_add_f32_e32 v16, v19, v8
	v_add_f32_e32 v17, v9, v16
	v_sub_f32_e32 v13, v9, v13
	v_sub_f32_e32 v13, v14, v13
	v_sub_f32_e32 v14, v16, v19
	v_sub_f32_e32 v18, v17, v9
	v_sub_f32_e32 v8, v8, v14
	v_sub_f32_e32 v16, v16, v18
	v_sub_f32_e32 v18, v17, v18
	v_add_f32_e32 v14, v13, v8
	v_sub_f32_e32 v9, v9, v18
	v_add_f32_e32 v9, v16, v9
	v_sub_f32_e32 v18, v14, v13
	v_add_f32_e32 v9, v14, v9
	v_sub_f32_e32 v14, v14, v18
	v_add_f32_e32 v16, v17, v9
	v_sub_f32_e32 v8, v8, v18
	v_sub_f32_e32 v13, v13, v14
	v_add_f32_e32 v8, v8, v13
	v_sub_f32_e32 v13, v16, v17
	v_sub_f32_e32 v9, v9, v13
	v_add_f32_e32 v8, v8, v9
	v_add_f32_e32 v8, v16, v8
	v_cmp_neq_f32_e32 vcc, s23, v15
	v_add_u32_e32 v13, -2, v222
	s_nop 0
	v_cndmask_b32_e32 v8, v219, v8, vcc
	v_cmp_ngt_f32_e32 vcc, -1.0, v15
	s_nop 1
	v_cndmask_b32_e32 v8, v220, v8, vcc
	v_cmp_neq_f32_e32 vcc, -1.0, v15
	s_nop 1
	v_cndmask_b32_e32 v8, v221, v8, vcc
	v_cmp_lt_f32_e64 vcc, |v15|, s6
	s_nop 1
	v_cndmask_b32_e32 v8, v8, v15, vcc
	v_add_f32_e32 v9, v12, v8
	v_sub_f32_e32 v8, v7, v10
	v_and_b32_e32 v12, 64, v222
	v_add_u32_e32 v10, -1, v222
	v_cmp_lt_i32_e32 vcc, v10, v12
	v_sub_f32_e32 v9, v8, v9
	s_nop 0
	v_cndmask_b32_e32 v10, v10, v222, vcc
	v_lshlrev_b32_e32 v10, 2, v10
	ds_bpermute_b32 v10, v10, v9
	v_cmp_eq_u32_e32 vcc, 0, v22
	s_waitcnt lgkmcnt(0)
	v_add_f32_e32 v10, v9, v10
	v_cndmask_b32_e32 v10, v10, v9, vcc
	v_cmp_lt_i32_e32 vcc, v13, v12
	s_nop 1
	v_cndmask_b32_e32 v13, v13, v222, vcc
	v_lshlrev_b32_e32 v13, 2, v13
	ds_bpermute_b32 v13, v13, v10
	v_cmp_gt_u32_e32 vcc, 2, v22
	s_waitcnt lgkmcnt(0)
	v_add_f32_e32 v13, v10, v13
	v_cndmask_b32_e32 v10, v13, v10, vcc
	v_add_u32_e32 v13, -4, v222
	v_cmp_lt_i32_e32 vcc, v13, v12
	s_nop 1
	v_cndmask_b32_e32 v13, v13, v222, vcc
	v_lshlrev_b32_e32 v13, 2, v13
	ds_bpermute_b32 v13, v13, v10
	v_cmp_gt_u32_e32 vcc, 4, v22
	s_waitcnt lgkmcnt(0)
	v_add_f32_e32 v13, v10, v13
	v_cndmask_b32_e32 v10, v13, v10, vcc
	v_add_u32_e32 v13, -8, v222
	v_cmp_lt_i32_e32 vcc, v13, v12
	s_nop 1
	v_cndmask_b32_e32 v13, v13, v222, vcc
	v_lshlrev_b32_e32 v13, 2, v13
	ds_bpermute_b32 v13, v13, v10
	v_cmp_gt_u32_e32 vcc, 8, v22
	s_waitcnt lgkmcnt(0)
	v_add_f32_e32 v13, v10, v13
	v_cndmask_b32_e32 v10, v13, v10, vcc
	v_add_u32_e32 v13, -16, v222
	v_cmp_lt_i32_e32 vcc, v13, v12
	s_nop 1
	v_cndmask_b32_e32 v13, v13, v222, vcc
	v_lshlrev_b32_e32 v13, 2, v13
	ds_bpermute_b32 v13, v13, v10
	v_cmp_gt_u32_e32 vcc, 16, v22
	s_waitcnt lgkmcnt(0)
	v_add_f32_e32 v13, v10, v13
	v_cndmask_b32_e32 v10, v13, v10, vcc
	v_subrev_u32_e32 v13, 32, v222
	v_cmp_lt_i32_e32 vcc, v13, v12
	s_nop 1
	v_cndmask_b32_e32 v12, v13, v222, vcc
	v_lshlrev_b32_e32 v12, 2, v12
	ds_bpermute_b32 v12, v12, v10
	v_cmp_eq_u32_e32 vcc, 63, v22
	s_waitcnt lgkmcnt(0)
	v_add_f32_e32 v12, v10, v12
	s_and_saveexec_b64 s[0:1], vcc
	s_lshl_b32 s6, s4, 2
	s_add_i32 s6, s6, 0
	v_mov_b32_e32 v13, s6
	ds_write_b32 v13, v12
	s_or_b64 exec, exec, s[0:1]
	v_cmp_gt_u32_e32 vcc, 32, v22
	s_cmp_lt_i32 s4, 1
	s_waitcnt lgkmcnt(0)
	v_cndmask_b32_e32 v10, v12, v10, vcc
	v_sub_f32_e32 v10, v10, v9
	s_barrier
	s_cbranch_scc1 .LBB0_445
	s_cmp_lt_u32 s4, 8
	s_mov_b32 s0, 0
	s_cbranch_scc1 .LBB0_442
	s_and_b32 s0, s4, 0x7ffffff8
	s_mov_b32 s1, 0
	s_mov_b32 s6, 0

.LBB0_445:
	v_readlane_b32 s0, v252, 2
	s_add_u32 s0, s2, s0
	s_addc_u32 s1, s3, 0
	v_readlane_b32 s5, v252, 4
	s_add_u32 s0, s0, s5
	s_addc_u32 s1, s1, 0
	v_lshl_add_u64 v[12:13], v[2:3], 2, s[0:1]
	v_pk_add_f32 v[16:17], v[10:11], v[0:1] op_sel_hi:[0,1]
	v_sub_f32_e32 v2, v10, v11
	v_mov_b32_e32 v3, v17
	v_pk_add_f32 v[4:5], v[4:5], v[10:11] op_sel_hi:[1,0]
	v_pk_add_f32 v[6:7], v[6:7], v[10:11] op_sel_hi:[1,0]
	v_pk_add_f32 v[8:9], v[8:9], v[10:11] op_sel_hi:[1,0]
	v_add_co_u32_e32 v10, vcc, 0x300000, v12
	s_mov_b64 s[0:1], 0x300000
	v_pk_mul_f32 v[4:5], v[4:5], s[22:23] op_sel_hi:[1,0]
	v_pk_mul_f32 v[2:3], v[2:3], s[22:23] op_sel_hi:[1,0]
	v_addc_co_u32_e32 v11, vcc, 0, v13, vcc
	v_lshl_add_u64 v[14:15], v[12:13], 0, s[0:1]
	v_pk_mul_f32 v[8:9], v[8:9], s[22:23] op_sel_hi:[1,0]
	v_pk_mul_f32 v[6:7], v[6:7], s[22:23] op_sel_hi:[1,0]
	global_store_dwordx4 v[10:11], v[2:5], off
	global_store_dwordx4 v[14:15], v[6:9], off offset:16
	s_branch .Lcs_return
